# adds GEMM1 tile transition: next tile's As[1][1] K-tile-1 half staged before the epilogue stores; peeled first K-iteration with vmcnt relaxed by the outstanding stores
# baseline (speedup 1.0000x reference)
.LBB0_185:
	s_mov_b32 s100, 0
	v_readlane_b32 s40, v237, 6
	s_lshl_b32 s8, s8, 5
	v_mov_b32_e32 v137, v3
	v_readlane_b32 s41, v237, 7
	s_and_b32 s11, s8, 0x60
	s_add_i32 m0, s60, 0x18000
	v_lshl_add_u64 v[4:5], v[4:5], 0, s[16:17]
	v_lshl_add_u64 v[16:17], s[40:41], 0, v[136:137]
	v_mov_b32_e32 v135, v3
	s_lshl_b32 s10, s7, 13
	s_lshl_b32 s12, s11, 7
	s_waitcnt vmcnt(2)
	s_barrier
	global_load_lds_dwordx4 v[4:5], off
	v_lshl_add_u64 v[4:5], v[6:7], 0, s[16:17]
	s_add_i32 m0, s60, 0x1a000
	s_add_i32 s82, s60, 0x8000
	s_add_i32 s83, s60, 0xa000
	v_lshl_add_u64 v[18:19], s[40:41], 0, v[134:135]
	global_load_lds_dwordx4 v[4:5], off
	v_lshl_add_u64 v[4:5], v[16:17], 0, s[16:17]
	s_mov_b32 m0, s82
	s_add_u32 s8, s42, 0x80080
	global_load_lds_dwordx4 v[4:5], off
	v_lshl_add_u64 v[4:5], v[18:19], 0, s[16:17]
	s_mov_b32 m0, s83
	s_addc_u32 s9, s43, 0
	global_load_lds_dwordx4 v[4:5], off
	s_add_i32 m0, s60, 0x1c000
	v_lshl_add_u64 v[4:5], s[8:9], 0, v[2:3]
	global_load_lds_dwordx4 v[4:5], off
	v_lshl_add_u64 v[4:5], s[8:9], 0, v[132:133]
	s_add_i32 m0, s60, 0x1e000
	s_cmpk_lt_u32 s6, 0x100
	global_load_lds_dwordx4 v[4:5], off
	v_lshrrev_b32_e32 v5, 1, v8
	v_and_b32_e32 v5, 24, v5
	v_and_b32_e32 v4, 15, v8
	v_lshlrev_b32_e32 v6, 1, v5
	v_lshl_or_b32 v1, s7, 6, v4
	v_lshl_or_b32 v4, v4, 6, v6
	v_lshlrev_b32_e32 v6, 2, v8
	v_and_b32_e32 v6, 32, v6
	v_bitop3_b32 v7, v4, s10, v6 bitop3:0xde
	v_bitop3_b32 v154, v4, s12, v6 bitop3:0xde
	v_or_b32_e32 v6, s11, v5
	v_lshlrev_b32_e32 v4, 1, v6
	v_mov_b32_e32 v5, v3
	v_lshl_add_u64 v[138:139], s[68:69], 0, v[4:5]
	v_lshlrev_b32_e32 v4, 2, v6
	v_lshl_add_u64 v[140:141], s[2:3], 0, v[4:5]
	v_lshlrev_b32_e32 v4, 15, v13
	v_and_b32_e32 v4, 0xffff0000, v4
	v_lshl_add_u32 v4, v12, 12, v4
	v_and_b32_e32 v5, 1, v13
	v_lshl_or_b32 v4, v5, 6, v4
	v_lshl_add_u32 v142, v14, 1, v4
	v_lshlrev_b32_e32 v4, 15, v9
	v_and_b32_e32 v4, 0xffff0000, v4
	s_waitcnt vmcnt(6)
	v_lshl_add_u32 v4, v10, 12, v4
	v_and_b32_e32 v5, 1, v9
	v_lshl_or_b32 v4, v5, 6, v4
	v_readlane_b32 s8, v238, 62
	s_cselect_b64 s[6:7], -1, 0
	v_mov_b32_e32 v143, v3
	v_lshl_add_u32 v144, v11, 1, v4
	v_mov_b32_e32 v145, v3
	s_mov_b32 s84, 0
	v_add_u32_e32 v155, 0, v7
	v_readlane_b32 s14, v238, 51
	s_mov_b32 s85, s8
	s_barrier
	v_readlane_b32 s9, v238, 63
	s_branch .LBB0_188

.LBB0_190:
	s_ashr_i32 s9, s8, 31
	s_lshl_b64 s[36:37], s[8:9], 20
	v_readlane_b32 s9, v239, 48
	s_add_u32 s36, s9, s36
	v_readlane_b32 s9, v237, 38
	s_addc_u32 s37, s9, s37
	s_and_b64 s[38:39], s[12:13], exec
	s_cselect_b32 s9, s37, s41
	s_cselect_b32 s86, s36, s40
	s_ashr_i32 s11, s10, 31
	s_lshl_b64 s[38:39], s[10:11], 20
	s_add_u32 s38, s48, s38
	s_addc_u32 s39, s49, s39
	s_and_b64 s[44:45], s[12:13], exec
	s_cselect_b32 s11, s39, s43
	s_cselect_b32 s87, s38, s42
	s_add_u32 s40, s40, 0x80080
	s_addc_u32 s41, s41, 0
	s_add_u32 s88, s42, 0x100
	v_mov_b32_e32 v4, 0
	s_addc_u32 s89, s43, 0
	s_mov_b32 s90, -2
	v_mov_b32_e32 v5, v4
	v_mov_b32_e32 v6, v4
	v_mov_b32_e32 v7, v4
	v_mov_b32_e32 v8, v4
	v_mov_b32_e32 v9, v4
	v_mov_b32_e32 v10, v4
	v_mov_b32_e32 v11, v4
	v_mov_b32_e32 v12, v4
	v_mov_b32_e32 v13, v4
	v_mov_b32_e32 v14, v4
	v_mov_b32_e32 v15, v4
	v_mov_b32_e32 v16, v4
	v_mov_b32_e32 v17, v4
	v_mov_b32_e32 v18, v4
	v_mov_b32_e32 v19, v4
	v_mov_b32_e32 v28, v4
	v_mov_b32_e32 v29, v4
	v_mov_b32_e32 v30, v4
	v_mov_b32_e32 v31, v4
	v_mov_b32_e32 v32, v4
	v_mov_b32_e32 v33, v4
	v_mov_b32_e32 v34, v4
	v_mov_b32_e32 v35, v4
	v_mov_b32_e32 v44, v4
	v_mov_b32_e32 v45, v4
	v_mov_b32_e32 v46, v4
	v_mov_b32_e32 v47, v4
	v_mov_b32_e32 v48, v4
	v_mov_b32_e32 v49, v4
	v_mov_b32_e32 v50, v4
	v_mov_b32_e32 v51, v4
	v_mov_b32_e32 v20, v4
	v_mov_b32_e32 v21, v4
	v_mov_b32_e32 v22, v4
	v_mov_b32_e32 v23, v4
	v_mov_b32_e32 v24, v4
	v_mov_b32_e32 v25, v4
	v_mov_b32_e32 v26, v4
	v_mov_b32_e32 v27, v4
	v_mov_b32_e32 v36, v4
	v_mov_b32_e32 v37, v4
	v_mov_b32_e32 v38, v4
	v_mov_b32_e32 v39, v4
	v_mov_b32_e32 v40, v4
	v_mov_b32_e32 v41, v4
	v_mov_b32_e32 v42, v4
	v_mov_b32_e32 v43, v4
	v_mov_b32_e32 v52, v4
	v_mov_b32_e32 v53, v4
	v_mov_b32_e32 v54, v4
	v_mov_b32_e32 v55, v4
	v_mov_b32_e32 v56, v4
	v_mov_b32_e32 v57, v4
	v_mov_b32_e32 v58, v4
	v_mov_b32_e32 v59, v4
	v_mov_b32_e32 v60, v4
	v_mov_b32_e32 v61, v4
	v_mov_b32_e32 v62, v4
	v_mov_b32_e32 v63, v4
	v_mov_b32_e32 v64, v4
	v_mov_b32_e32 v65, v4
	v_mov_b32_e32 v66, v4
	v_mov_b32_e32 v67, v4
	v_mov_b32_e32 v68, v4
	v_mov_b32_e32 v69, v4
	v_mov_b32_e32 v70, v4
	v_mov_b32_e32 v71, v4
	v_mov_b32_e32 v72, v4
	v_mov_b32_e32 v73, v4
	v_mov_b32_e32 v74, v4
	v_mov_b32_e32 v75, v4
	v_mov_b32_e32 v76, v4
	v_mov_b32_e32 v77, v4
	v_mov_b32_e32 v78, v4
	v_mov_b32_e32 v79, v4
	v_mov_b32_e32 v80, v4
	v_mov_b32_e32 v81, v4
	v_mov_b32_e32 v82, v4
	v_mov_b32_e32 v83, v4
	v_mov_b32_e32 v84, v4
	v_mov_b32_e32 v85, v4
	v_mov_b32_e32 v86, v4
	v_mov_b32_e32 v87, v4
	v_mov_b32_e32 v92, v4
	v_mov_b32_e32 v93, v4
	v_mov_b32_e32 v94, v4
	v_mov_b32_e32 v95, v4
	v_mov_b32_e32 v100, v4
	v_mov_b32_e32 v101, v4
	v_mov_b32_e32 v102, v4
	v_mov_b32_e32 v103, v4
	v_mov_b32_e32 v108, v4
	v_mov_b32_e32 v109, v4
	v_mov_b32_e32 v110, v4
	v_mov_b32_e32 v111, v4
	v_mov_b32_e32 v88, v4
	v_mov_b32_e32 v89, v4
	v_mov_b32_e32 v90, v4
	v_mov_b32_e32 v91, v4
	v_mov_b32_e32 v96, v4
	v_mov_b32_e32 v97, v4
	v_mov_b32_e32 v98, v4
	v_mov_b32_e32 v99, v4
	v_mov_b32_e32 v104, v4
	v_mov_b32_e32 v105, v4
	v_mov_b32_e32 v106, v4
	v_mov_b32_e32 v107, v4
	v_mov_b32_e32 v112, v4
	v_mov_b32_e32 v113, v4
	v_mov_b32_e32 v114, v4
	v_mov_b32_e32 v115, v4
	v_mov_b32_e32 v116, v4
	v_mov_b32_e32 v117, v4
	v_mov_b32_e32 v118, v4
	v_mov_b32_e32 v119, v4
	v_mov_b32_e32 v120, v4
	v_mov_b32_e32 v121, v4
	v_mov_b32_e32 v122, v4
	v_mov_b32_e32 v123, v4
	v_mov_b32_e32 v124, v4
	v_mov_b32_e32 v125, v4
	v_mov_b32_e32 v126, v4
	v_mov_b32_e32 v127, v4
	v_mov_b32_e32 v128, v4
	v_mov_b32_e32 v129, v4
	v_mov_b32_e32 v130, v4
	v_mov_b32_e32 v131, v4
	s_cmp_eq_u32 s100, 1
	s_cbranch_scc0 .LBB0_191
	s_add_u32 s42, s40, 0xfff80080
	s_addc_u32 s43, s41, -1
	s_add_i32 s91, 0, 0x10000
	s_cmp_eq_u32 s90, 28
	s_cselect_b32 s45, s9, s43
	s_cselect_b32 s44, s86, s42
	s_cselect_b32 s43, s11, s89
	s_cselect_b32 s42, s87, s88
	s_add_i32 s94, 0, 0x14000
	v_add_u32_e32 v160, s91, v154
	v_add_u32_e32 v176, s94, v154
	ds_read_b128 v[146:149], v160
	ds_read_b128 v[150:153], v160 offset:1024
	ds_read_b128 v[156:159], v160 offset:2048
	ds_read_b128 v[160:163], v160 offset:3072
	ds_read_b128 v[164:167], v176
	ds_read_b128 v[168:171], v176 offset:1024
	ds_read_b128 v[172:175], v176 offset:2048
	ds_read_b128 v[176:179], v176 offset:3072
	ds_read_b128 v[180:183], v155
	ds_read_b128 v[184:187], v155 offset:1024
	ds_read_b128 v[188:191], v155 offset:2048
	ds_read_b128 v[192:195], v155 offset:3072
	ds_read_b128 v[196:199], v155 offset:4096
	ds_read_b128 v[200:203], v155 offset:5120
	ds_read_b128 v[204:207], v155 offset:6144
	ds_read_b128 v[218:221], v155 offset:7168
	s_waitcnt vmcnt(24)
	s_waitcnt lgkmcnt(0)
	s_barrier
	s_setprio 1
	s_waitcnt lgkmcnt(0)
	v_mfma_f32_16x16x32_bf16 v[128:131], v[146:149], v[180:183], v[128:131]
	v_mfma_f32_16x16x32_bf16 v[124:127], v[156:159], v[180:183], v[124:127]
	v_mfma_f32_16x16x32_bf16 v[120:123], v[146:149], v[188:191], v[120:123]
	v_mfma_f32_16x16x32_bf16 v[116:119], v[156:159], v[188:191], v[116:119]
	v_mfma_f32_16x16x32_bf16 v[112:115], v[146:149], v[196:199], v[112:115]
	v_mfma_f32_16x16x32_bf16 v[104:107], v[156:159], v[196:199], v[104:107]
	v_mfma_f32_16x16x32_bf16 v[96:99], v[146:149], v[204:207], v[96:99]
	v_mfma_f32_16x16x32_bf16 v[88:91], v[156:159], v[204:207], v[88:91]
	v_mfma_f32_16x16x32_bf16 v[128:131], v[150:153], v[184:187], v[128:131]
	v_mfma_f32_16x16x32_bf16 v[124:127], v[160:163], v[184:187], v[124:127]
	v_mfma_f32_16x16x32_bf16 v[120:123], v[150:153], v[192:195], v[120:123]
	v_mfma_f32_16x16x32_bf16 v[116:119], v[160:163], v[192:195], v[116:119]
	v_mfma_f32_16x16x32_bf16 v[112:115], v[150:153], v[200:203], v[112:115]
	v_mfma_f32_16x16x32_bf16 v[104:107], v[160:163], v[200:203], v[104:107]
	v_mfma_f32_16x16x32_bf16 v[96:99], v[150:153], v[218:221], v[96:99]
	v_mfma_f32_16x16x32_bf16 v[88:91], v[160:163], v[218:221], v[88:91]
	s_setprio 0
	s_setprio 1
	v_mfma_f32_16x16x32_bf16 v[108:111], v[164:167], v[180:183], v[108:111]
	v_mfma_f32_16x16x32_bf16 v[100:103], v[172:175], v[180:183], v[100:103]
	v_mfma_f32_16x16x32_bf16 v[92:95], v[164:167], v[188:191], v[92:95]
	v_mfma_f32_16x16x32_bf16 v[84:87], v[172:175], v[188:191], v[84:87]
	v_mfma_f32_16x16x32_bf16 v[80:83], v[164:167], v[196:199], v[80:83]
	v_mfma_f32_16x16x32_bf16 v[76:79], v[172:175], v[196:199], v[76:79]
	v_mfma_f32_16x16x32_bf16 v[72:75], v[164:167], v[204:207], v[72:75]
	v_mfma_f32_16x16x32_bf16 v[68:71], v[172:175], v[204:207], v[68:71]
	v_mfma_f32_16x16x32_bf16 v[108:111], v[168:171], v[184:187], v[108:111]
	v_mfma_f32_16x16x32_bf16 v[100:103], v[176:179], v[184:187], v[100:103]
	v_mfma_f32_16x16x32_bf16 v[92:95], v[168:171], v[192:195], v[92:95]
	v_mfma_f32_16x16x32_bf16 v[84:87], v[176:179], v[192:195], v[84:87]
	v_mfma_f32_16x16x32_bf16 v[80:83], v[168:171], v[200:203], v[80:83]
	v_mfma_f32_16x16x32_bf16 v[76:79], v[176:179], v[200:203], v[76:79]
	v_mfma_f32_16x16x32_bf16 v[72:75], v[168:171], v[218:221], v[72:75]
	v_mfma_f32_16x16x32_bf16 v[68:71], v[176:179], v[218:221], v[68:71]
	s_setprio 0
	s_barrier
	s_add_i32 s91, s91, s51
	v_lshl_add_u64 v[222:223], s[42:43], 0, v[2:3]
	s_mov_b32 m0, s91
	ds_read_b128 v[180:183], v155 offset:16384
	ds_read_b128 v[184:187], v155 offset:17408
	ds_read_b128 v[188:191], v155 offset:18432
	ds_read_b128 v[192:195], v155 offset:19456
	ds_read_b128 v[196:199], v155 offset:20480
	ds_read_b128 v[200:203], v155 offset:21504
	ds_read_b128 v[204:207], v155 offset:22528
	ds_read_b128 v[218:221], v155 offset:23552
	global_load_lds_dwordx4 v[222:223], off
	s_add_i32 m0, s91, 0x2000
	s_add_u32 s92, s42, 0x80000
	v_lshl_add_u64 v[224:225], s[42:43], 0, v[132:133]
	s_addc_u32 s93, s43, 0
	s_add_i32 s91, s94, s51
	global_load_lds_dwordx4 v[224:225], off
	v_lshl_add_u64 v[226:227], s[92:93], 0, v[2:3]
	s_mov_b32 m0, s91
	v_lshl_add_u64 v[228:229], s[44:45], 0, v[134:135]
	global_load_lds_dwordx4 v[226:227], off
	v_lshl_add_u64 v[226:227], s[92:93], 0, v[132:133]
	s_add_i32 m0, s91, 0x2000
	s_nop 0
	global_load_lds_dwordx4 v[226:227], off
	v_lshl_add_u64 v[226:227], s[44:45], 0, v[136:137]
	s_mov_b32 m0, s60
	s_nop 0
	global_load_lds_dwordx4 v[226:227], off
	s_mov_b32 m0, s61
	s_nop 0
	global_load_lds_dwordx4 v[228:229], off
	s_waitcnt vmcnt(24)
	s_waitcnt lgkmcnt(0)
	s_barrier
	s_setprio 1
	s_waitcnt lgkmcnt(0)
	v_mfma_f32_16x16x32_bf16 v[64:67], v[146:149], v[180:183], v[64:67]
	v_mfma_f32_16x16x32_bf16 v[60:63], v[156:159], v[180:183], v[60:63]
	v_mfma_f32_16x16x32_bf16 v[56:59], v[146:149], v[188:191], v[56:59]
	v_mfma_f32_16x16x32_bf16 v[52:55], v[156:159], v[188:191], v[52:55]
	v_mfma_f32_16x16x32_bf16 v[40:43], v[146:149], v[196:199], v[40:43]
	v_mfma_f32_16x16x32_bf16 v[36:39], v[156:159], v[196:199], v[36:39]
	v_mfma_f32_16x16x32_bf16 v[24:27], v[146:149], v[204:207], v[24:27]
	v_mfma_f32_16x16x32_bf16 v[20:23], v[156:159], v[204:207], v[20:23]
	v_mfma_f32_16x16x32_bf16 v[64:67], v[150:153], v[184:187], v[64:67]
	v_mfma_f32_16x16x32_bf16 v[60:63], v[160:163], v[184:187], v[60:63]
	v_mfma_f32_16x16x32_bf16 v[56:59], v[150:153], v[192:195], v[56:59]
	v_mfma_f32_16x16x32_bf16 v[52:55], v[160:163], v[192:195], v[52:55]
	v_mfma_f32_16x16x32_bf16 v[40:43], v[150:153], v[200:203], v[40:43]
	v_mfma_f32_16x16x32_bf16 v[36:39], v[160:163], v[200:203], v[36:39]
	v_mfma_f32_16x16x32_bf16 v[24:27], v[150:153], v[218:221], v[24:27]
	v_mfma_f32_16x16x32_bf16 v[20:23], v[160:163], v[218:221], v[20:23]
	s_setprio 0
	s_setprio 1
	v_mfma_f32_16x16x32_bf16 v[48:51], v[164:167], v[180:183], v[48:51]
	v_mfma_f32_16x16x32_bf16 v[44:47], v[172:175], v[180:183], v[44:47]
	v_mfma_f32_16x16x32_bf16 v[32:35], v[164:167], v[188:191], v[32:35]
	v_mfma_f32_16x16x32_bf16 v[28:31], v[172:175], v[188:191], v[28:31]
	v_mfma_f32_16x16x32_bf16 v[16:19], v[164:167], v[196:199], v[16:19]
	v_mfma_f32_16x16x32_bf16 v[12:15], v[172:175], v[196:199], v[12:15]
	v_mfma_f32_16x16x32_bf16 v[8:11], v[164:167], v[204:207], v[8:11]
	v_mfma_f32_16x16x32_bf16 v[4:7], v[172:175], v[204:207], v[4:7]
	v_mfma_f32_16x16x32_bf16 v[48:51], v[168:171], v[184:187], v[48:51]
	v_mfma_f32_16x16x32_bf16 v[44:47], v[176:179], v[184:187], v[44:47]
	v_mfma_f32_16x16x32_bf16 v[32:35], v[168:171], v[192:195], v[32:35]
	v_mfma_f32_16x16x32_bf16 v[28:31], v[176:179], v[192:195], v[28:31]
	v_mfma_f32_16x16x32_bf16 v[16:19], v[168:171], v[200:203], v[16:19]
	v_mfma_f32_16x16x32_bf16 v[12:15], v[176:179], v[200:203], v[12:15]
	v_mfma_f32_16x16x32_bf16 v[8:11], v[168:171], v[218:221], v[8:11]
	v_mfma_f32_16x16x32_bf16 v[4:7], v[176:179], v[218:221], v[4:7]
	s_setprio 0
	s_barrier
	s_add_i32 s91, 0, 0x18000
	s_add_i32 s92, 0, 0x1c000
	v_add_u32_e32 v160, s91, v154
	v_add_u32_e32 v176, s92, v154
	ds_read_b128 v[146:149], v160
	ds_read_b128 v[150:153], v160 offset:1024
	ds_read_b128 v[156:159], v160 offset:2048
	ds_read_b128 v[160:163], v160 offset:3072
	ds_read_b128 v[164:167], v176
	ds_read_b128 v[168:171], v176 offset:1024
	ds_read_b128 v[172:175], v176 offset:2048
	ds_read_b128 v[176:179], v176 offset:3072
	s_add_u32 s44, s44, 0x80000
	s_addc_u32 s45, s45, 0
	s_mov_b32 m0, s80
	v_lshl_add_u64 v[230:231], s[44:45], 0, v[136:137]
	ds_read_b128 v[180:183], v155 offset:32768
	ds_read_b128 v[184:187], v155 offset:33792
	ds_read_b128 v[188:191], v155 offset:34816
	ds_read_b128 v[192:195], v155 offset:35840
	ds_read_b128 v[196:199], v155 offset:36864
	ds_read_b128 v[200:203], v155 offset:37888
	ds_read_b128 v[204:207], v155 offset:38912
	ds_read_b128 v[218:221], v155 offset:39936
	global_load_lds_dwordx4 v[230:231], off
	v_lshl_add_u64 v[230:231], s[44:45], 0, v[134:135]
	s_mov_b32 m0, s81
	s_nop 0
	global_load_lds_dwordx4 v[230:231], off
	s_waitcnt vmcnt(24)
	s_waitcnt lgkmcnt(0)
	s_barrier
	s_setprio 1
	s_waitcnt lgkmcnt(0)
	v_mfma_f32_16x16x32_bf16 v[128:131], v[146:149], v[180:183], v[128:131]
	v_mfma_f32_16x16x32_bf16 v[124:127], v[156:159], v[180:183], v[124:127]
	v_mfma_f32_16x16x32_bf16 v[120:123], v[146:149], v[188:191], v[120:123]
	v_mfma_f32_16x16x32_bf16 v[116:119], v[156:159], v[188:191], v[116:119]
	v_mfma_f32_16x16x32_bf16 v[112:115], v[146:149], v[196:199], v[112:115]
	v_mfma_f32_16x16x32_bf16 v[104:107], v[156:159], v[196:199], v[104:107]
	v_mfma_f32_16x16x32_bf16 v[96:99], v[146:149], v[204:207], v[96:99]
	v_mfma_f32_16x16x32_bf16 v[88:91], v[156:159], v[204:207], v[88:91]
	v_mfma_f32_16x16x32_bf16 v[128:131], v[150:153], v[184:187], v[128:131]
	v_mfma_f32_16x16x32_bf16 v[124:127], v[160:163], v[184:187], v[124:127]
	v_mfma_f32_16x16x32_bf16 v[120:123], v[150:153], v[192:195], v[120:123]
	v_mfma_f32_16x16x32_bf16 v[116:119], v[160:163], v[192:195], v[116:119]
	v_mfma_f32_16x16x32_bf16 v[112:115], v[150:153], v[200:203], v[112:115]
	v_mfma_f32_16x16x32_bf16 v[104:107], v[160:163], v[200:203], v[104:107]
	v_mfma_f32_16x16x32_bf16 v[96:99], v[150:153], v[218:221], v[96:99]
	v_mfma_f32_16x16x32_bf16 v[88:91], v[160:163], v[218:221], v[88:91]
	s_setprio 0
	s_setprio 1
	v_mfma_f32_16x16x32_bf16 v[108:111], v[164:167], v[180:183], v[108:111]
	v_mfma_f32_16x16x32_bf16 v[100:103], v[172:175], v[180:183], v[100:103]
	v_mfma_f32_16x16x32_bf16 v[92:95], v[164:167], v[188:191], v[92:95]
	v_mfma_f32_16x16x32_bf16 v[84:87], v[172:175], v[188:191], v[84:87]
	v_mfma_f32_16x16x32_bf16 v[80:83], v[164:167], v[196:199], v[80:83]
	v_mfma_f32_16x16x32_bf16 v[76:79], v[172:175], v[196:199], v[76:79]
	v_mfma_f32_16x16x32_bf16 v[72:75], v[164:167], v[204:207], v[72:75]
	v_mfma_f32_16x16x32_bf16 v[68:71], v[172:175], v[204:207], v[68:71]
	v_mfma_f32_16x16x32_bf16 v[108:111], v[168:171], v[184:187], v[108:111]
	v_mfma_f32_16x16x32_bf16 v[100:103], v[176:179], v[184:187], v[100:103]
	v_mfma_f32_16x16x32_bf16 v[92:95], v[168:171], v[192:195], v[92:95]
	v_mfma_f32_16x16x32_bf16 v[84:87], v[176:179], v[192:195], v[84:87]
	v_mfma_f32_16x16x32_bf16 v[80:83], v[168:171], v[200:203], v[80:83]
	v_mfma_f32_16x16x32_bf16 v[76:79], v[176:179], v[200:203], v[76:79]
	v_mfma_f32_16x16x32_bf16 v[72:75], v[168:171], v[218:221], v[72:75]
	v_mfma_f32_16x16x32_bf16 v[68:71], v[176:179], v[218:221], v[68:71]
	s_setprio 0
	s_barrier
	s_add_i32 s44, s91, s51
	v_lshl_add_u64 v[222:223], v[222:223], 0, s[16:17]
	s_mov_b32 m0, s44
	ds_read_b128 v[180:183], v155 offset:49152
	ds_read_b128 v[184:187], v155 offset:50176
	ds_read_b128 v[188:191], v155 offset:51200
	ds_read_b128 v[192:195], v155 offset:52224
	ds_read_b128 v[196:199], v155 offset:53248
	ds_read_b128 v[200:203], v155 offset:54272
	ds_read_b128 v[204:207], v155 offset:55296
	ds_read_b128 v[218:221], v155 offset:56320
	global_load_lds_dwordx4 v[222:223], off
	s_add_i32 m0, s44, 0x2000
	s_add_u32 s42, s42, 0x80080
	v_lshl_add_u64 v[222:223], v[224:225], 0, s[16:17]
	s_addc_u32 s43, s43, 0
	s_add_i32 s44, s92, s51
	global_load_lds_dwordx4 v[222:223], off
	v_lshl_add_u64 v[222:223], s[42:43], 0, v[2:3]
	s_mov_b32 m0, s44
	s_nop 0
	global_load_lds_dwordx4 v[222:223], off
	v_lshl_add_u64 v[222:223], s[42:43], 0, v[132:133]
	s_add_i32 m0, s44, 0x2000
	s_nop 0
	global_load_lds_dwordx4 v[222:223], off
	v_lshl_add_u64 v[222:223], v[226:227], 0, s[16:17]
	s_mov_b32 m0, s82
	s_nop 0
	global_load_lds_dwordx4 v[222:223], off
	v_lshl_add_u64 v[222:223], v[228:229], 0, s[16:17]
	s_mov_b32 m0, s83
	s_nop 0
	global_load_lds_dwordx4 v[222:223], off
	s_waitcnt vmcnt(8)
	s_waitcnt lgkmcnt(0)
	s_barrier
	s_setprio 1
	s_waitcnt lgkmcnt(0)
	v_mfma_f32_16x16x32_bf16 v[64:67], v[146:149], v[180:183], v[64:67]
	v_mfma_f32_16x16x32_bf16 v[60:63], v[156:159], v[180:183], v[60:63]
	v_mfma_f32_16x16x32_bf16 v[56:59], v[146:149], v[188:191], v[56:59]
	v_mfma_f32_16x16x32_bf16 v[52:55], v[156:159], v[188:191], v[52:55]
	v_mfma_f32_16x16x32_bf16 v[40:43], v[146:149], v[196:199], v[40:43]
	v_mfma_f32_16x16x32_bf16 v[36:39], v[156:159], v[196:199], v[36:39]
	v_mfma_f32_16x16x32_bf16 v[24:27], v[146:149], v[204:207], v[24:27]
	v_mfma_f32_16x16x32_bf16 v[20:23], v[156:159], v[204:207], v[20:23]
	v_mfma_f32_16x16x32_bf16 v[64:67], v[150:153], v[184:187], v[64:67]
	v_mfma_f32_16x16x32_bf16 v[60:63], v[160:163], v[184:187], v[60:63]
	v_mfma_f32_16x16x32_bf16 v[56:59], v[150:153], v[192:195], v[56:59]
	v_mfma_f32_16x16x32_bf16 v[52:55], v[160:163], v[192:195], v[52:55]
	v_mfma_f32_16x16x32_bf16 v[40:43], v[150:153], v[200:203], v[40:43]
	v_mfma_f32_16x16x32_bf16 v[36:39], v[160:163], v[200:203], v[36:39]
	v_mfma_f32_16x16x32_bf16 v[24:27], v[150:153], v[218:221], v[24:27]
	v_mfma_f32_16x16x32_bf16 v[20:23], v[160:163], v[218:221], v[20:23]
	s_setprio 0
	s_setprio 1
	v_mfma_f32_16x16x32_bf16 v[48:51], v[164:167], v[180:183], v[48:51]
	v_mfma_f32_16x16x32_bf16 v[44:47], v[172:175], v[180:183], v[44:47]
	v_mfma_f32_16x16x32_bf16 v[32:35], v[164:167], v[188:191], v[32:35]
	v_mfma_f32_16x16x32_bf16 v[28:31], v[172:175], v[188:191], v[28:31]
	v_mfma_f32_16x16x32_bf16 v[16:19], v[164:167], v[196:199], v[16:19]
	v_mfma_f32_16x16x32_bf16 v[12:15], v[172:175], v[196:199], v[12:15]
	v_mfma_f32_16x16x32_bf16 v[8:11], v[164:167], v[204:207], v[8:11]
	v_mfma_f32_16x16x32_bf16 v[4:7], v[172:175], v[204:207], v[4:7]
	v_mfma_f32_16x16x32_bf16 v[48:51], v[168:171], v[184:187], v[48:51]
	v_mfma_f32_16x16x32_bf16 v[44:47], v[176:179], v[184:187], v[44:47]
	v_mfma_f32_16x16x32_bf16 v[32:35], v[168:171], v[192:195], v[32:35]
	v_mfma_f32_16x16x32_bf16 v[28:31], v[176:179], v[192:195], v[28:31]
	v_mfma_f32_16x16x32_bf16 v[16:19], v[168:171], v[200:203], v[16:19]
	v_mfma_f32_16x16x32_bf16 v[12:15], v[176:179], v[200:203], v[12:15]
	v_mfma_f32_16x16x32_bf16 v[8:11], v[168:171], v[218:221], v[8:11]
	v_mfma_f32_16x16x32_bf16 v[4:7], v[176:179], v[218:221], v[4:7]
	s_setprio 0
	s_barrier
	s_add_i32 s90, s90, 2
	s_add_u32 s40, s40, 0x100
	s_addc_u32 s41, s41, 0
	s_add_u32 s88, s88, 0x100
	s_addc_u32 s89, s89, 0

.LBB0_194:
	s_add_u32 s98, s86, 0x80080
	s_addc_u32 s99, s9, 0
	v_lshl_add_u64 v[222:223], s[98:99], 0, v[142:143]
	s_add_i32 m0, s60, 0xc000
	s_nop 0
	global_load_lds_dwordx4 v[222:223], off
	v_lshl_add_u64 v[222:223], s[98:99], 0, v[144:145]
	s_add_i32 m0, s60, 0xe000
	s_nop 0
	global_load_lds_dwordx4 v[222:223], off
	s_mov_b32 s100, 1
	v_lshl_add_u32 v152, s85, 8, v1
	s_lshl_b32 s40, s14, 8
	s_cmp_lt_i32 s14, 58
	s_mov_b64 s[42:43], -1
	v_or_b32_e32 v150, 16, v152
	v_or_b32_e32 v148, 32, v152
	v_or_b32_e32 v146, 48, v152
	s_cbranch_scc0 .LBB0_196
	s_ashr_i32 s41, s40, 31
	v_lshl_add_u64 v[160:161], s[40:41], 1, v[138:139]
	s_movk_i32 s9, 0x7400
	v_mad_i64_i32 v[162:163], s[42:43], v152, s9, v[160:161]
	v_cvt_pk_bf16_f32 v156, v128, v129
	v_cvt_pk_bf16_f32 v157, v130, v131
	v_cvt_pk_bf16_f32 v158, v124, v125
	v_cvt_pk_bf16_f32 v159, v126, v127
	global_store_dwordx4 v[162:163], v[156:159], off
	v_add_u32_e32 v147, 0x80, v152
	s_nop 0
	v_cvt_pk_bf16_f32 v156, v108, v109
	v_cvt_pk_bf16_f32 v157, v110, v111
	v_cvt_pk_bf16_f32 v158, v100, v101
	v_cvt_pk_bf16_f32 v159, v102, v103
	global_store_dwordx4 v[162:163], v[156:159], off offset:256
	v_mad_i64_i32 v[162:163], s[42:43], v150, s9, v[160:161]
	s_nop 0
	v_cvt_pk_bf16_f32 v156, v120, v121
	v_cvt_pk_bf16_f32 v157, v122, v123
	v_cvt_pk_bf16_f32 v158, v116, v117
	v_cvt_pk_bf16_f32 v159, v118, v119
	global_store_dwordx4 v[162:163], v[156:159], off
	s_nop 1
	v_cvt_pk_bf16_f32 v156, v92, v93
	v_cvt_pk_bf16_f32 v157, v94, v95
	v_cvt_pk_bf16_f32 v158, v84, v85
	v_cvt_pk_bf16_f32 v159, v86, v87
	global_store_dwordx4 v[162:163], v[156:159], off offset:256
	v_mad_i64_i32 v[162:163], s[42:43], v148, s9, v[160:161]
	s_nop 0
	v_cvt_pk_bf16_f32 v156, v112, v113
	v_cvt_pk_bf16_f32 v157, v114, v115
	v_cvt_pk_bf16_f32 v158, v104, v105
	v_cvt_pk_bf16_f32 v159, v106, v107
	global_store_dwordx4 v[162:163], v[156:159], off
	s_nop 1
	v_cvt_pk_bf16_f32 v156, v80, v81
	v_cvt_pk_bf16_f32 v157, v82, v83
	v_cvt_pk_bf16_f32 v158, v76, v77
	v_cvt_pk_bf16_f32 v159, v78, v79
	global_store_dwordx4 v[162:163], v[156:159], off offset:256
	v_mad_i64_i32 v[162:163], s[42:43], v146, s9, v[160:161]
	s_nop 0
	v_cvt_pk_bf16_f32 v156, v96, v97
	v_cvt_pk_bf16_f32 v157, v98, v99
	v_cvt_pk_bf16_f32 v158, v88, v89
	v_cvt_pk_bf16_f32 v159, v90, v91
	global_store_dwordx4 v[162:163], v[156:159], off
	s_nop 1
	v_cvt_pk_bf16_f32 v156, v72, v73
	v_cvt_pk_bf16_f32 v157, v74, v75
	v_cvt_pk_bf16_f32 v158, v68, v69
	v_cvt_pk_bf16_f32 v159, v70, v71
	global_store_dwordx4 v[162:163], v[156:159], off offset:256
	v_mad_i64_i32 v[162:163], s[42:43], v147, s9, v[160:161]
	s_nop 0
	v_cvt_pk_bf16_f32 v156, v64, v65
	v_cvt_pk_bf16_f32 v157, v66, v67
	v_cvt_pk_bf16_f32 v158, v60, v61
	v_cvt_pk_bf16_f32 v159, v62, v63
	global_store_dwordx4 v[162:163], v[156:159], off
	v_add_u32_e32 v147, 0x90, v152
	s_nop 0
	v_cvt_pk_bf16_f32 v156, v48, v49
	v_cvt_pk_bf16_f32 v157, v50, v51
	v_cvt_pk_bf16_f32 v158, v44, v45
	v_cvt_pk_bf16_f32 v159, v46, v47
	global_store_dwordx4 v[162:163], v[156:159], off offset:256
	v_mad_i64_i32 v[162:163], s[42:43], v147, s9, v[160:161]
	s_nop 0
	v_cvt_pk_bf16_f32 v156, v56, v57
	v_cvt_pk_bf16_f32 v157, v58, v59
	v_cvt_pk_bf16_f32 v158, v52, v53
	v_cvt_pk_bf16_f32 v159, v54, v55
	global_store_dwordx4 v[162:163], v[156:159], off
	v_add_u32_e32 v147, 0xa0, v152
	s_nop 0
	v_cvt_pk_bf16_f32 v156, v32, v33
	v_cvt_pk_bf16_f32 v157, v34, v35
	v_cvt_pk_bf16_f32 v158, v28, v29
	v_cvt_pk_bf16_f32 v159, v30, v31
	global_store_dwordx4 v[162:163], v[156:159], off offset:256
	v_mad_i64_i32 v[162:163], s[42:43], v147, s9, v[160:161]
	s_nop 0
	v_cvt_pk_bf16_f32 v156, v40, v41
	v_cvt_pk_bf16_f32 v157, v42, v43
	v_cvt_pk_bf16_f32 v158, v36, v37
	v_cvt_pk_bf16_f32 v159, v38, v39
	global_store_dwordx4 v[162:163], v[156:159], off
	v_add_u32_e32 v147, 0xb0, v152
	v_mad_i64_i32 v[160:161], s[42:43], v147, s9, v[160:161]
	v_cvt_pk_bf16_f32 v156, v16, v17
	v_cvt_pk_bf16_f32 v157, v18, v19
	v_cvt_pk_bf16_f32 v158, v12, v13
	v_cvt_pk_bf16_f32 v159, v14, v15
	global_store_dwordx4 v[162:163], v[156:159], off offset:256
	s_mov_b64 s[42:43], 0
	s_nop 0
	v_cvt_pk_bf16_f32 v156, v24, v25
	v_cvt_pk_bf16_f32 v157, v26, v27
	v_cvt_pk_bf16_f32 v158, v20, v21
	v_cvt_pk_bf16_f32 v159, v22, v23
	global_store_dwordx4 v[160:161], v[156:159], off
	s_nop 1
	v_cvt_pk_bf16_f32 v156, v8, v9
	v_cvt_pk_bf16_f32 v157, v10, v11
	v_cvt_pk_bf16_f32 v158, v4, v5
	v_cvt_pk_bf16_f32 v159, v6, v7
	global_store_dwordx4 v[160:161], v[156:159], off offset:256

	.amdhsa_kernel _Z3fwd4Args
		.amdhsa_group_segment_fixed_size 0
		.amdhsa_private_segment_fixed_size 0
		.amdhsa_kernarg_size 480
		.amdhsa_user_sgpr_count 2
		.amdhsa_user_sgpr_dispatch_ptr 0
		.amdhsa_user_sgpr_queue_ptr 0
		.amdhsa_user_sgpr_kernarg_segment_ptr 1
		.amdhsa_user_sgpr_dispatch_id 0
		.amdhsa_user_sgpr_kernarg_preload_length 0
		.amdhsa_user_sgpr_kernarg_preload_offset 0
		.amdhsa_user_sgpr_private_segment_size 0
		.amdhsa_uses_dynamic_stack 0
		.amdhsa_enable_private_segment 0
		.amdhsa_system_sgpr_workgroup_id_x 1
		.amdhsa_system_sgpr_workgroup_id_y 0
		.amdhsa_system_sgpr_workgroup_id_z 0
		.amdhsa_system_sgpr_workgroup_info 0
		.amdhsa_system_vgpr_workitem_id 0
		.amdhsa_next_free_vgpr 256
		.amdhsa_next_free_sgpr 102
		.amdhsa_accum_offset 256
		.amdhsa_reserve_vcc 1
		.amdhsa_float_round_mode_32 0
		.amdhsa_float_round_mode_16_64 0
		.amdhsa_float_denorm_mode_32 3
		.amdhsa_float_denorm_mode_16_64 3
		.amdhsa_dx10_clamp 1
		.amdhsa_ieee_mode 1
		.amdhsa_fp16_overflow 0
		.amdhsa_tg_split 0
		.amdhsa_exception_fp_ieee_invalid_op 0
		.amdhsa_exception_fp_denorm_src 0
		.amdhsa_exception_fp_ieee_div_zero 0
		.amdhsa_exception_fp_ieee_overflow 0
		.amdhsa_exception_fp_ieee_underflow 0
		.amdhsa_exception_fp_ieee_inexact 0
		.amdhsa_exception_int_div_zero 0
	.end_amdhsa_kernel

amdhsa.kernels:
  - .agpr_count:     0
    .args:
      - .offset:         0
        .size:           224
        .value_kind:     by_value
      - .offset:         224
        .size:           4
        .value_kind:     hidden_block_count_x
      - .offset:         228
        .size:           4
        .value_kind:     hidden_block_count_y
      - .offset:         232
        .size:           4
        .value_kind:     hidden_block_count_z
      - .offset:         236
        .size:           2
        .value_kind:     hidden_group_size_x
      - .offset:         238
        .size:           2
        .value_kind:     hidden_group_size_y
      - .offset:         240
        .size:           2
        .value_kind:     hidden_group_size_z
      - .offset:         242
        .size:           2
        .value_kind:     hidden_remainder_x
      - .offset:         244
        .size:           2
        .value_kind:     hidden_remainder_y
      - .offset:         246
        .size:           2
        .value_kind:     hidden_remainder_z
      - .offset:         264
        .size:           8
        .value_kind:     hidden_global_offset_x
      - .offset:         272
        .size:           8
        .value_kind:     hidden_global_offset_y
      - .offset:         280
        .size:           8
        .value_kind:     hidden_global_offset_z
      - .offset:         288
        .size:           2
        .value_kind:     hidden_grid_dims
      - .offset:         344
        .size:           4
        .value_kind:     hidden_dynamic_lds_size
    .group_segment_fixed_size: 0
    .kernarg_segment_align: 8
    .kernarg_segment_size: 480
    .language:       OpenCL C
    .language_version:
      - 2
      - 0
    .max_flat_workgroup_size: 512
    .name:           _Z3fwd4Args
    .private_segment_fixed_size: 0
    .sgpr_count:     108
    .sgpr_spill_count: 488
    .symbol:         _Z3fwd4Args.kd
    .uniform_work_group_size: 1
    .uses_dynamic_stack: false
    .vgpr_count:     256
    .vgpr_spill_count: 0
    .wavefront_size: 64
